# 4096 more layer-1 expert weight items moved out of the prologue into staggered slots of layer 0's FFN-up/FFN-down phases (WGs 0-127 convert at phase start, WGs 128-255 at phase end, one item per wave
# speedup vs baseline: 1.0453x; 1.0052x over previous
.LBB0_13:
	s_mov_b32 s101, 0
	v_writelane_b32 v253, s11, 8
	s_movk_i32 s2, 0x80
	v_writelane_b32 v253, s10, 9
	v_cmp_gt_i32_e32 vcc, s2, v1
	s_and_saveexec_b64 s[4:5], vcc
	s_cbranch_execz .LBB0_15
	v_cvt_f32_i32_e32 v2, v1
	s_mov_b32 s2, 0x7f800000
	v_mov_b32_e32 v8, 0xbf1f24be
	v_mul_f32_e32 v2, 0x3c800000, v2
	v_mul_f32_e64 v3, |v2|, 0.5
	v_fract_f32_e32 v4, v3
	v_add_f32_e32 v4, v4, v4
	v_cmp_neq_f32_e32 vcc, s2, v3
	v_cmp_gt_f32_e64 s[2:3], |v2|, 1.0
	v_and_b32_e32 v6, 0x7fffffff, v2
	v_cndmask_b32_e32 v3, 0, v4, vcc
	v_cndmask_b32_e64 v3, |v2|, v3, s[2:3]
	v_add_f32_e32 v4, v3, v3
	v_rndne_f32_e32 v4, v4
	v_fmac_f32_e32 v3, -0.5, v4
	v_cvt_i32_f32_e32 v5, v4
	v_mul_f32_e32 v4, v3, v3
	v_fmac_f32_e32 v8, 0x3e75aa41, v4
	v_fmaak_f32 v8, v4, v8, 0x40234736
	v_fmaak_f32 v8, v4, v8, 0xc0a55e0e
	v_mul_f32_e32 v9, v3, v4
	v_mul_f32_e32 v8, v9, v8
	v_fmamk_f32 v3, v3, 0x40490fdb, v8
	v_mov_b32_e32 v8, 0x3e642e9d
	v_fmac_f32_e32 v8, 0x3d4be544, v4
	v_fmaak_f32 v8, v4, v8, 0xbfaad1da
	v_fmaak_f32 v8, v4, v8, 0x4081e0d3
	v_fmaak_f32 v8, v4, v8, 0xc09de9e6
	v_fma_f32 v4, v4, v8, 1.0
	v_and_b32_e32 v8, 1, v5
	v_and_b32_e32 v7, 2, v5
	v_cmp_eq_u32_e32 vcc, 0, v8
	v_cmp_eq_u32_e64 s[2:3], 0, v7
	v_lshl_add_u32 v9, v1, 2, 0
	v_cndmask_b32_e64 v8, -v3, v4, vcc
	v_cndmask_b32_e64 v7, -v8, v8, s[2:3]
	s_movk_i32 s2, 0x1f8
	v_cndmask_b32_e32 v3, v4, v3, vcc
	v_lshlrev_b32_e32 v4, 30, v5
	v_cmp_class_f32_e64 s[2:3], v2, s2
	v_and_b32_e32 v4, 0x80000000, v4
	v_xor_b32_e32 v2, v6, v2
	v_xor_b32_e32 v2, v2, v4
	v_mov_b32_e32 v8, 0x7fc00000
	v_xor_b32_e32 v2, v2, v3
	v_cndmask_b32_e64 v7, v8, v7, s[2:3]
	v_add_u32_e32 v9, 0x21000, v9
	v_cndmask_b32_e64 v2, v8, v2, s[2:3]
	ds_write2st64_b32 v9, v7, v2 offset1:2

.LBB0_41:
	v_writelane_b32 v253, s24, 32
	v_writelane_b32 v253, s23, 34
	v_writelane_b32 v253, s22, 36
	s_mov_b32 s3, 0
	v_readlane_b32 s0, v253, 29
	s_lshl_b32 s0, s0, 14
	s_add_i32 s29, s0, 0
	s_cmp_lg_u64 s[48:49], 0
	v_readlane_b32 s4, v253, 30
	s_cselect_b64 s[44:45], -1, 0
	s_abs_i32 s2, s4
	v_cvt_f32_u32_e32 v2, s2
	s_sub_i32 s0, 0, s2
	s_ashr_i32 s6, s4, 31
	v_rcp_iflag_f32_e32 v2, v2
	s_nop 0
	v_mul_f32_e32 v2, 0x4f7ffffe, v2
	v_cvt_u32_f32_e32 v2, v2
	s_nop 0
	v_readfirstlane_b32 s1, v2
	s_mul_i32 s0, s0, s1
	s_mul_hi_u32 s0, s1, s0
	s_add_i32 s7, s1, s0
	s_mul_hi_u32 s0, s7, 0x4200
	s_mul_i32 s0, s0, s2
	s_sub_i32 s0, 0x4200, s0
	s_sub_i32 s1, s0, s2
	s_cmp_ge_u32 s0, s2
	s_cselect_b32 s0, s1, s0
	s_sub_i32 s1, s0, s2
	s_cmp_ge_u32 s0, s2
	s_cselect_b32 s8, s1, s0
	s_add_i32 s0, s4, 0xffffff00
	s_cmp_ge_i32 s0, s8
	s_cselect_b64 s[0:1], -1, 0
	s_cmpk_lt_u32 s8, 0x2101
	s_cselect_b64 s[4:5], -1, 0
	s_sub_i32 s8, 0x4200, s8
	s_and_b64 s[0:1], s[0:1], s[4:5]
	s_and_b64 s[0:1], s[0:1], exec
	s_cselect_b32 s5, s8, 0x4200
	s_add_i32 s0, s5, 0xffffe200
	s_cmp_eq_u32 s2, 0x800
	s_cselect_b32 s5, s0, s5
	v_writelane_b32 v253, s5, 38
	v_writelane_b32 v253, s48, 40
	s_mul_hi_u32 s0, s5, s7
	s_mul_i32 s1, s0, s2
	v_writelane_b32 v253, s49, 41
	v_writelane_b32 v253, s50, 42
	v_writelane_b32 v253, s51, 43
	v_writelane_b32 v253, s52, 44
	v_writelane_b32 v253, s53, 45
	v_writelane_b32 v253, s54, 46
	v_writelane_b32 v253, s55, 47
	s_sub_i32 s1, s5, s1
	v_writelane_b32 v253, s56, 48
	s_add_i32 s4, s0, 1
	s_sub_i32 s5, s1, s2
	v_writelane_b32 v253, s57, 49
	s_cmp_ge_u32 s1, s2
	v_writelane_b32 v253, s58, 50
	s_cselect_b32 s0, s4, s0
	v_writelane_b32 v253, s59, 51
	s_cselect_b32 s1, s5, s1
	s_add_i32 s4, s0, 1
	v_writelane_b32 v253, s60, 52
	s_cmp_ge_u32 s1, s2
	v_writelane_b32 v253, s61, 53
	s_cselect_b32 s0, s4, s0
	v_writelane_b32 v253, s62, 54
	s_xor_b32 s0, s0, s6
	v_writelane_b32 v253, s63, 55
	s_sub_i32 s15, s0, s6
	v_writelane_b32 v253, s29, 56
	s_add_i32 s14, s15, -1
	v_writelane_b32 v253, s44, 57
	s_cmp_lt_i32 s15, 1
	v_readfirstlane_b32 s0, v0
	v_writelane_b32 v253, s45, 58
	s_cbranch_scc1 .LBB0_65
	s_ashr_i32 s0, s0, 6
	s_min_i32 s18, s0, s14
	s_cmpk_gt_i32 s27, 0x7ff
	v_readlane_b32 s0, v253, 26
	s_cselect_b64 s[20:21], -1, 0
	s_add_u32 s0, s0, 0x800000
	v_writelane_b32 v253, s0, 59
	v_mov_b32_e32 v133, 0
	v_readlane_b32 s0, v253, 27
	s_addc_u32 s0, s0, 0
	s_add_i32 s25, 0, 0x21000
	v_writelane_b32 v253, s0, 61
	s_add_i32 s0, 0, 0x21200
	v_writelane_b32 v253, s0, 63
	s_add_i32 s0, 0, 0x21100
	v_writelane_b32 v254, s0, 1
	s_add_i32 s0, 0, 0x21300
	v_writelane_b32 v254, s0, 3
	v_writelane_b32 v254, s27, 5
	v_writelane_b32 v254, s14, 7
	v_writelane_b32 v254, s15, 9
	v_writelane_b32 v254, s18, 11
	v_writelane_b32 v254, s20, 13
	s_mov_b32 s22, 0x42800000
	s_mov_b32 s19, 0
	v_writelane_b32 v254, s21, 14
	s_branch .LBB0_45

.LBB0_893:
	s_cmp_eq_u32 s101, 0
	s_cbranch_scc1 .Lfret_none
	s_cmp_eq_u32 s101, 1
	s_cbranch_scc1 .Lfret_1
	s_cmp_eq_u32 s101, 2
	s_cbranch_scc1 .Lfret_2
	s_cmp_eq_u32 s101, 3
	s_cbranch_scc1 .Lfret_3
	s_branch .Lfret_4

.LBB0_947:
	s_or_b64 exec, exec, s[30:31]
	v_mov_b32_e32 v6, v0
	s_mov_b64 s[0:1], 0
	v_readlane_b32 s36, v253, 8
	s_waitcnt lgkmcnt(0)
	s_barrier
	v_readlane_b32 s1, v253, 9
	s_cmpk_lg_i32 s1, 0x100
	s_cbranch_scc1 .Lfs1_skip
	v_readlane_b32 s1, v254, 20
	s_cmp_eq_u32 s1, 0
	s_cbranch_scc1 .Lfs1_skip
	s_cmpk_gt_i32 s36, 0x7f
	s_cbranch_scc1 .Lfs1_skip
	v_readfirstlane_b32 s1, v0
	s_lshl_b32 s0, s36, 3
	s_lshr_b32 s1, s1, 6
	s_add_i32 s0, s0, s1
	s_addk_i32 s0, 0x2e00
	s_mov_b32 s101, 1
	v_readlane_b32 s62, v253, 54
	v_readlane_b32 s26, v253, 55
	s_mov_b32 s73, 0x10000
	v_mov_b32_e32 v135, v0
	v_and_b32_e32 v132, 63, v0
	s_branch .Ltkf_go
.Lfret_1:
	s_mov_b32 s101, 0
	s_waitcnt vmcnt(0) lgkmcnt(0)
	s_barrier
.Lfs1_skip:
	v_mov_b32_e32 v6, v0
	s_mov_b64 s[0:1], 0
	s_cmpk_lt_i32 s36, 0x1600
	v_readfirstlane_b32 s4, v6
	s_cbranch_scc0 .LBB0_972
	v_bfe_i32 v4, v6, 27, 1
	v_lshlrev_b32_e32 v2, 4, v6
	v_lshrrev_b32_e32 v4, 22, v4
	v_add_u32_e32 v4, v2, v4
	v_and_b32_e32 v4, 0xfffffc00, v4
	v_sub_u32_e32 v4, v2, v4
	v_readlane_b32 s8, v253, 40
	v_ashrrev_i32_e32 v3, 31, v6
	v_lshrrev_b32_e32 v5, 4, v4
	v_readlane_b32 s22, v253, 54
	v_lshrrev_b32_e32 v3, 26, v3
	v_bitop3_b32 v4, v5, v4, 32 bitop3:0x6c
	v_readlane_b32 s23, v253, 55
	s_add_u32 s5, s22, s0
	v_add_u32_e32 v3, v6, v3
	v_ashrrev_i32_e32 v7, 31, v4
	s_addc_u32 s1, s23, s1
	v_ashrrev_i32_e32 v3, 6, v3
	v_lshrrev_b32_e32 v7, 26, v7
	s_add_u32 s6, s5, 0x23000000
	v_lshlrev_b32_e32 v5, 3, v3
	v_add_u32_e32 v8, v4, v7
	s_addc_u32 s7, s1, 0
	v_and_b32_e32 v5, -16, v5
	v_ashrrev_i32_e32 v9, 6, v8
	s_add_u32 s0, s5, s97
	v_add_u32_e32 v7, v9, v5
	v_and_b32_e32 v5, 0xc0, v8
	s_addc_u32 s2, s1, 0
	v_sub_u32_e32 v4, v4, v5
	s_add_u32 s38, s0, 0xc00000
	v_lshlrev_b32_e32 v3, 5, v3
	v_ashrrev_i16_sdwa v4, v237, sext(v4) dst_sel:DWORD dst_unused:UNUSED_PAD src0_sel:DWORD src1_sel:BYTE_0
	v_lshlrev_b32_e32 v5, 1, v7
	v_lshrrev_b32_e32 v8, 2, v7
	v_and_b32_e32 v9, 3, v9
	s_mov_b32 s0, 0x3fffe0
	v_and_b32_e32 v3, 32, v3
	v_bfe_i32 v4, v4, 0, 16
	v_and_b32_e32 v5, 24, v5
	v_and_b32_e32 v8, 4, v8
	v_and_or_b32 v9, v7, s0, v9
	v_add_u32_e32 v2, 0x2000, v2
	v_or3_b32 v5, v9, v8, v5
	v_add_lshl_u32 v8, v3, v4, 1
	v_ashrrev_i32_e32 v3, 31, v2
	v_lshrrev_b32_e32 v3, 22, v3
	v_add_u32_e32 v3, v2, v3
	v_ashrrev_i32_e32 v3, 10, v3
	v_mul_i32_i24_e32 v4, 0x400, v3
	v_sub_u32_e32 v2, v2, v4
	v_lshrrev_b32_e32 v4, 4, v2
	v_bitop3_b32 v2, v4, v2, 32 bitop3:0x6c
	v_lshl_add_u32 v194, v5, 10, v8
	v_ashrrev_i32_e32 v5, 31, v2
	v_lshrrev_b32_e32 v5, 26, v5
	s_addc_u32 s39, s2, 0
	v_lshlrev_b32_e32 v4, 3, v3
	v_add_u32_e32 v5, v2, v5
	v_readlane_b32 s9, v253, 41
	s_add_u32 s8, s5, 0x170000
	v_and_b32_e32 v4, -16, v4
	v_ashrrev_i32_e32 v10, 6, v5
	s_addc_u32 s9, s1, 0
	v_add_u32_e32 v9, v10, v4
	v_and_b32_e32 v10, 3, v10
	s_ashr_i32 s40, s36, 31
	v_and_or_b32 v10, v9, s0, v10
	s_lshr_b32 s0, s40, 29
	v_readlane_b32 s17, v253, 49
	v_and_b32_e32 v4, 0xc0, v5
	s_add_i32 s0, s36, s0
	v_readlane_b32 s10, v253, 42
	v_readlane_b32 s16, v253, 48
	v_sub_u32_e32 v2, v2, v4
	s_ashr_i32 s17, s4, 6
	s_ashr_i32 s2, s0, 3
	s_and_b32 s0, s0, -8
	s_ashr_i32 s16, s4, 8
	v_lshlrev_b32_e32 v3, 5, v3
	v_ashrrev_i16_sdwa v2, v237, sext(v2) dst_sel:DWORD dst_unused:UNUSED_PAD src0_sel:DWORD src1_sel:BYTE_0
	v_lshlrev_b32_e32 v4, 1, v9
	v_lshrrev_b32_e32 v5, 2, v9
	s_lshl_b32 s10, s17, 10
	s_sub_i32 s0, s36, s0
	v_and_b32_e32 v3, 32, v3
	v_bfe_i32 v2, v2, 0, 16
	v_and_b32_e32 v4, 24, v4
	v_and_b32_e32 v5, 4, v5
	s_cmp_lt_i32 s0, 0
	s_movk_i32 s3, 0x2c1
	v_or3_b32 v4, v10, v5, v4
	v_add_lshl_u32 v10, v3, v2, 1
	s_cselect_b32 s3, s3, 0x2c0
	v_mov_b32_e32 v2, v0
	s_mul_i32 s0, s3, s0
	s_add_i32 s0, s0, s2
	v_ashrrev_i32_e32 v3, 31, v2
	v_lshrrev_b32_e32 v3, 26, v3
	s_mul_hi_i32 s2, s0, 0x2e8ba2e9
	v_lshlrev_b32_e32 v12, 4, v2
	v_add_u32_e32 v3, v2, v3
	v_bfe_i32 v2, v2, 27, 1
	s_lshr_b32 s3, s2, 31
	s_ashr_i32 s2, s2, 4
	v_lshrrev_b32_e32 v2, 22, v2
	s_add_i32 s2, s2, s3
	v_add_u32_e32 v2, v12, v2
	s_lshl_b32 s3, s2, 2
	s_mulk_i32 s2, 0x58
	v_and_b32_e32 v2, 0xfffffc00, v2
	s_sub_i32 s2, s0, s2
	v_sub_u32_e32 v2, v12, v2
	v_lshl_add_u32 v162, v4, 10, v10
	s_bfe_i32 s0, s2, 0x80000
	v_lshrrev_b32_e32 v4, 4, v2
	v_readlane_b32 s11, v253, 43
	s_bfe_u32 s0, s0, 0x2000d
	v_bitop3_b32 v2, v4, v2, 32 bitop3:0x6c
	s_add_i32 s11, s2, s0
	v_ashrrev_i32_e32 v5, 31, v2
	s_bfe_i32 s0, s11, 0x80000
	s_and_b32 s11, s11, 0xfc
	v_lshrrev_b32_e32 v5, 26, v5
	s_sub_i32 s2, s2, s11
	v_add_u32_e32 v5, v2, v5
	s_sext_i32_i8 s2, s2
	v_ashrrev_i32_e32 v3, 6, v3
	v_ashrrev_i32_e32 v11, 6, v5
	v_and_b32_e32 v5, 0xc0, v5
	v_readlane_b32 s13, v253, 45
	s_add_i32 s55, s3, s2
	v_lshlrev_b32_e32 v4, 3, v3
	v_sub_u32_e32 v2, v2, v5
	s_lshl_b32 s13, s55, 8
	v_and_b32_e32 v4, -16, v4
	v_lshlrev_b32_e32 v3, 5, v3
	v_ashrrev_i16_sdwa v2, v237, sext(v2) dst_sel:DWORD dst_unused:UNUSED_PAD src0_sel:DWORD src1_sel:BYTE_0
	v_and_b32_e32 v3, 32, v3
	v_bfe_i32 v5, v2, 0, 16
	v_add3_u32 v2, v4, s13, v11
	v_add_lshl_u32 v11, v3, v5, 1
	v_ashrrev_i32_e32 v3, 31, v2
	v_lshl_add_u64 v[4:5], v[2:3], 2, s[8:9]
	global_load_dword v3, v[4:5], off
	global_load_dword v13, v[4:5], off offset:512
	v_add_u32_e32 v2, 0x80, v2
	s_sext_i32_i16 s0, s0
	v_readlane_b32 s12, v253, 44
	s_lshr_b32 s0, s0, 2
	s_ashr_i32 s12, s55, 4
	s_bfe_i64 s[2:3], s[0:1], 0x100000
	s_mul_hi_i32 s11, s12, 0x580000
	s_mul_i32 s12, s12, 0x580000
	s_lshl_b64 s[2:3], s[2:3], 18
	s_add_u32 s12, s38, s12
	s_addc_u32 s11, s39, s11
	s_add_u32 s12, s12, s2
	v_mov_b32_e32 v163, v195
	v_readlane_b32 s14, v253, 46
	v_readlane_b32 s15, v253, 47
	v_readlane_b32 s18, v253, 50
	v_readlane_b32 s19, v253, 51
	v_readlane_b32 s20, v253, 52
	v_readlane_b32 s21, v253, 53
	s_waitcnt vmcnt(0)
	v_lshl_add_u32 v164, v3, 10, v11
	v_lshl_add_u32 v11, v13, 10, v11
	v_add_u32_e32 v2, 0x2000, v12
	v_ashrrev_i32_e32 v3, 31, v2
	v_lshrrev_b32_e32 v3, 22, v3
	v_add_u32_e32 v3, v2, v3
	v_ashrrev_i32_e32 v3, 10, v3
	v_mul_i32_i24_e32 v4, 0x400, v3
	v_sub_u32_e32 v2, v2, v4
	v_lshrrev_b32_e32 v4, 4, v2
	v_bitop3_b32 v2, v4, v2, 32 bitop3:0x6c
	v_ashrrev_i32_e32 v5, 31, v2
	v_lshrrev_b32_e32 v5, 26, v5
	v_add_u32_e32 v5, v2, v5
	v_ashrrev_i32_e32 v12, 6, v5
	v_and_b32_e32 v5, 0xc0, v5
	v_lshlrev_b32_e32 v4, 3, v3
	v_sub_u32_e32 v2, v2, v5
	v_and_b32_e32 v4, -16, v4
	v_lshlrev_b32_e32 v3, 5, v3
	v_ashrrev_i16_sdwa v2, v237, sext(v2) dst_sel:DWORD dst_unused:UNUSED_PAD src0_sel:DWORD src1_sel:BYTE_0
	v_and_b32_e32 v3, 32, v3
	v_bfe_i32 v5, v2, 0, 16
	v_add3_u32 v2, v4, s13, v12
	v_add_lshl_u32 v12, v3, v5, 1
	v_ashrrev_i32_e32 v3, 31, v2
	v_lshl_add_u64 v[4:5], v[2:3], 2, s[8:9]
	global_load_dword v3, v[4:5], off
	global_load_dword v14, v[4:5], off offset:512
	v_add_u32_e32 v2, 0x80, v2
	s_addc_u32 s13, s11, s3
	s_add_i32 s41, s10, 0
	s_add_i32 s42, s41, 0x10000
	s_add_i32 s43, s41, 0x12000
	s_mov_b32 m0, s42
	s_add_u32 s2, s12, 0x20000
	s_addc_u32 s3, s13, 0
	s_add_i32 s44, s41, 0x14000
	s_add_i32 s45, s41, 0x16000
	s_add_i32 s46, s41, 0x2000
	s_add_i32 s47, s41, 0x4000
	s_add_i32 s48, s41, 0x6000
	s_cmp_eq_u32 s16, 1
	v_lshl_add_u64 v[4:5], s[12:13], 0, v[162:163]
	s_cselect_b64 s[10:11], -1, 0
	s_cmp_lg_u32 s16, 1
	s_waitcnt vmcnt(0)
	v_lshl_add_u32 v166, v3, 10, v12
	s_waitcnt vmcnt(0)
	global_load_lds_dwordx4 v194, s[12:13]
	s_mov_b32 m0, s43
	v_lshl_add_u32 v168, v14, 10, v12
	global_load_lds_dwordx4 v162, s[12:13]
	s_mov_b32 m0, s44
	v_lshl_add_u64 v[2:3], s[12:13], 0, v[194:195]
	global_load_lds_dwordx4 v194, s[2:3]
	s_mov_b32 m0, s45
	s_nop 0
	global_load_lds_dwordx4 v162, s[2:3]
	s_mov_b32 m0, s41
	s_nop 0
	global_load_lds_dwordx4 v164, s[6:7]
	s_mov_b32 m0, s46
	s_nop 0
	global_load_lds_dwordx4 v166, s[6:7]
	s_mov_b32 m0, s47
	s_nop 0
	global_load_lds_dwordx4 v11, s[6:7]
	s_mov_b32 m0, s48
	s_nop 0
	global_load_lds_dwordx4 v168, s[6:7]
	s_cbranch_scc1 .LBB0_950
	s_barrier

.LBB0_971:
	s_waitcnt vmcnt(0)
	s_barrier
	v_readlane_b32 s1, v253, 9
	s_cmpk_lg_i32 s1, 0x100
	s_cbranch_scc1 .Lfs2_skip
	v_readlane_b32 s1, v254, 20
	s_cmp_eq_u32 s1, 0
	s_cbranch_scc1 .Lfs2_skip
	v_readlane_b32 s27, v253, 8
	s_cmpk_lt_i32 s27, 0x80
	s_cbranch_scc1 .Lfs2_skip
	v_readfirstlane_b32 s1, v0
	s_lshl_b32 s0, s27, 3
	s_lshr_b32 s1, s1, 6
	s_add_i32 s0, s0, s1
	s_addk_i32 s0, 0x2600
	s_mov_b32 s101, 2
	v_readlane_b32 s62, v253, 54
	v_readlane_b32 s26, v253, 55
	s_mov_b32 s73, 0x10000
	v_mov_b32_e32 v135, v0
	v_and_b32_e32 v132, 63, v0
	s_branch .Ltkf_go
.Lfret_2:
	s_mov_b32 s101, 0
	s_waitcnt vmcnt(0) lgkmcnt(0)
.Lfs2_skip:
.LBB0_972:
	s_getreg_b32 s0, hwreg(HW_REG_XCC_ID, 0, 4)
	s_waitcnt vmcnt(0)
	s_waitcnt vmcnt(0) lgkmcnt(0)
	s_barrier
	s_mov_b64 s[2:3], exec
	v_readlane_b32 s4, v253, 4
	v_readlane_b32 s5, v253, 5
	s_and_b64 s[4:5], s[2:3], s[4:5]
	s_xor_b64 s[30:31], s[4:5], s[2:3]
	v_readlane_b32 s37, v253, 9
	s_mov_b64 exec, s[4:5]
	s_cbranch_execz .LBB0_1026
	v_readlane_b32 s1, v254, 24
	s_waitcnt vmcnt(0) expcnt(0) lgkmcnt(0)
	s_and_b32 s36, s0, 15
	v_mov_b32_e32 v2, s1
	ds_read_b32 v4, v2
	v_readlane_b32 s1, v254, 17
	s_waitcnt lgkmcnt(0)
	v_cmp_ne_u32_e32 vcc, 0, v4
	v_mov_b32_e32 v2, s1
	ds_read_b32 v2, v2
	s_cbranch_vccnz .LBB0_989
	v_readlane_b32 s2, v253, 0
	v_readlane_b32 s3, v253, 1
	s_load_dwordx2 s[0:1], s[2:3], 0x4
	s_mov_b32 s16, 1
	s_waitcnt lgkmcnt(0)
	s_mul_i32 s17, s0, s37
	s_mul_i32 s17, s17, s1
	s_mov_b64 s[0:1], 0
	s_branch .LBB0_977

.LBB0_1026:
	s_or_b64 exec, exec, s[30:31]
	v_mov_b32_e32 v10, v0
	s_mov_b64 s[0:1], 0
	v_readlane_b32 s24, v253, 8
	s_mov_b32 s25, s37
	s_waitcnt lgkmcnt(0)
	s_barrier
	v_readlane_b32 s1, v253, 9
	s_cmpk_lg_i32 s1, 0x100
	s_cbranch_scc1 .Lfs3_skip
	v_readlane_b32 s1, v254, 20
	s_cmp_eq_u32 s1, 0
	s_cbranch_scc1 .Lfs3_skip
	s_cmpk_gt_i32 s24, 0x7f
	s_cbranch_scc1 .Lfs3_skip
	v_readfirstlane_b32 s1, v0
	s_lshl_b32 s0, s24, 3
	s_lshr_b32 s1, s1, 6
	s_add_i32 s0, s0, s1
	s_addk_i32 s0, 0x2600
	s_mov_b32 s101, 3
	v_readlane_b32 s62, v253, 54
	v_readlane_b32 s26, v253, 55
	s_mov_b32 s73, 0x10000
	v_mov_b32_e32 v135, v0
	v_and_b32_e32 v132, 63, v0
	s_branch .Ltkf_go

.Lfs3_skip:
	v_mov_b32_e32 v10, v0
	s_mov_b64 s[0:1], 0
	v_readlane_b32 s24, v253, 8
	s_mov_b32 s25, s37
	s_cmpk_lt_i32 s24, 0x400
	v_readfirstlane_b32 s4, v10
	s_cbranch_scc0 .LBB0_1056
	s_ashr_i32 s26, s24, 31
	s_lshr_b32 s2, s26, 29
	s_add_i32 s7, s24, s2
	s_and_b32 s2, s7, -8
	s_sub_i32 s5, s24, s2
	s_cmp_gt_i32 s5, -1
	s_mov_b64 s[2:3], -1
	s_cbranch_scc0 .LBB0_1029
	s_lshl_b32 s6, s5, 7
	s_mov_b64 s[2:3], 0

.LBB0_1055:
	s_waitcnt vmcnt(0)
	v_readlane_b32 s37, v253, 9
	s_barrier
	v_readlane_b32 s1, v253, 9
	s_cmpk_lg_i32 s1, 0x100
	s_cbranch_scc1 .Lfs4_skip
	v_readlane_b32 s1, v254, 20
	s_cmp_eq_u32 s1, 0
	s_cbranch_scc1 .Lfs4_skip
	v_readlane_b32 s27, v253, 8
	s_cmpk_lt_i32 s27, 0x80
	s_cbranch_scc1 .Lfs4_skip
	v_readfirstlane_b32 s1, v0
	s_lshl_b32 s0, s27, 3
	s_lshr_b32 s1, s1, 6
	s_add_i32 s0, s0, s1
	s_addk_i32 s0, 0x1e00
	s_mov_b32 s101, 4
	v_readlane_b32 s62, v253, 54
	v_readlane_b32 s26, v253, 55
	s_mov_b32 s73, 0x10000
	v_mov_b32_e32 v135, v0
	v_and_b32_e32 v132, 63, v0
	s_branch .Ltkf_go

.Lfs4_skip:
.LBB0_1056:
	s_getreg_b32 s0, hwreg(HW_REG_XCC_ID, 0, 4)
	s_waitcnt vmcnt(0)
	s_waitcnt lgkmcnt(0)
	s_barrier
	s_mov_b64 s[2:3], exec
	v_readlane_b32 s4, v253, 4
	v_readlane_b32 s5, v253, 5
	s_and_b64 s[4:5], s[2:3], s[4:5]
	s_xor_b64 s[30:31], s[4:5], s[2:3]
	s_mov_b64 exec, s[4:5]
	s_cbranch_execnz .LBB0_1057
	s_getpc_b64 s[98:99]
